# prep: touch loads issued only by the eight waves that are idle after the barrier (nothing on the second-stage waves' path); rest as v46
# speedup vs baseline: 1.0175x; 1.0164x over previous
.Lprep_ld_done:
	s_getpc_b64 s[22:23]
	s_and_b32 s22, s22, 0xffffff00
	s_waitcnt vmcnt(0)
	v_pk_mul_f32 v[12:13], v[12:13], v[16:17] op_sel_hi:[1,0]
	v_pk_mul_f32 v[14:15], v[14:15], v[16:17] op_sel_hi:[1,0]
	v_pk_fma_f32 v[8:9], v[8:9], v[6:7], v[12:13] op_sel_hi:[1,0,1]
	v_pk_fma_f32 v[10:11], v[10:11], v[6:7], v[14:15] op_sel_hi:[1,0,1]
	s_nop 1
	v_permlane32_swap_b32_e32 v8, v10
	v_permlane32_swap_b32_e32 v9, v11
	v_add_f32_e32 v8, v8, v10
	v_add_f32_e32 v9, v9, v11
	s_nop 1
	v_permlane16_swap_b32_e32 v8, v9
	v_add_f32_e32 v8, v8, v9
	s_nop 1
	v_add_f32_dpp v8, v8, v8 row_ror:8 row_mask:0xf bank_mask:0xf bound_ctrl:1
	v_cmp_eq_u32_e32 vcc, 0, v39
	s_and_saveexec_b64 s[20:21], vcc
	ds_write_b32 v38, v8
	s_mov_b64 exec, s[20:21]
	s_cmp_lg_u32 s2, 0
	s_cbranch_scc1 .Lprep_bar
	v_mul_f32_e32 v23, v23, v24
	s_nop 1
	v_add_f32_dpp v23, v23, v23 quad_perm:[1,0,3,2] row_mask:0xf bank_mask:0xf bound_ctrl:1
	s_nop 1
	v_add_f32_dpp v23, v23, v23 quad_perm:[2,3,0,1] row_mask:0xf bank_mask:0xf bound_ctrl:1
	s_nop 1
	v_add_f32_dpp v23, v23, v23 row_ror:4 row_mask:0xf bank_mask:0xf bound_ctrl:1
	s_nop 1
	v_add_f32_dpp v23, v23, v23 row_ror:8 row_mask:0xf bank_mask:0xf bound_ctrl:1
	v_mov_b32_e32 v24, v23
	s_nop 1
	v_permlane16_swap_b32_e32 v23, v24
	v_add_f32_e32 v23, v23, v24
	v_mov_b32_e32 v24, v23
	s_nop 1
	v_permlane32_swap_b32_e32 v23, v24
	v_add_f32_e32 v23, v23, v24
	v_lshlrev_b32_e32 v22, 2, v20
	v_cmp_eq_u32_e32 vcc, 0, v19
	s_and_saveexec_b64 s[20:21], vcc
	ds_write_b32 v22, v23 offset:2048
	s_mov_b64 exec, s[20:21]
.Lprep_bar:
	s_waitcnt lgkmcnt(0)
	s_barrier
	v_readfirstlane_b32 s26, v20
	s_cmp_ge_u32 s26, 8
	s_cbranch_scc1 .Lprep_touch
	s_cmp_lt_u32 s14, 32
	s_cbranch_scc1 .Lprep_hid
	v_cmp_gt_u32_e32 vcc, 32, v0
	s_and_saveexec_b64 s[20:21], vcc
	s_cbranch_execz .Lprep_done
	v_lshlrev_b32_e32 v1, 2, v0
	ds_read2_b32 v[2:3], v1 offset1:32
	ds_read2_b32 v[4:5], v1 offset0:64 offset1:96
	ds_read2_b32 v[6:7], v1 offset0:128 offset1:160
	ds_read2_b32 v[8:9], v1 offset0:192 offset1:224
	v_add_u32_e32 v10, 0x400, v1
	ds_read2_b32 v[12:13], v10 offset1:32
	ds_read2_b32 v[14:15], v10 offset0:64 offset1:96
	ds_read2_b32 v[16:17], v10 offset0:128 offset1:160
	ds_read2_b32 v[18:19], v10 offset0:192 offset1:224
	s_lshl_b32 s16, s15, 12
	s_add_i32 s16, s16, s17
	s_sub_i32 s16, s16, 0x1000
	v_add_u32_e32 v1, s16, v1
	s_waitcnt lgkmcnt(6)
	v_pk_add_f32 v[2:3], v[2:3], v[4:5]
	s_waitcnt lgkmcnt(4)
	v_pk_add_f32 v[6:7], v[6:7], v[8:9]
	s_waitcnt lgkmcnt(2)
	v_pk_add_f32 v[12:13], v[12:13], v[14:15]
	s_waitcnt lgkmcnt(0)
	v_pk_add_f32 v[16:17], v[16:17], v[18:19]
	v_pk_add_f32 v[2:3], v[2:3], v[6:7]
	v_pk_add_f32 v[12:13], v[12:13], v[16:17]
	s_nop 0
	v_pk_add_f32 v[2:3], v[2:3], v[12:13]
	s_nop 0
	v_add_f32_e32 v6, v2, v3
	global_store_dword v1, v6, s[12:13]
	s_branch .Lprep_done

.Lprep_touch:
	v_subrev_u32_e32 v30, 0x200, v0
	v_lshlrev_b32_e32 v25, 4, v30
	global_load_dwordx4 v[26:29], v25, s[22:23]
	v_cmp_gt_u32_e32 vcc, 0x80, v30
	s_and_saveexec_b64 s[20:21], vcc
	s_cbranch_execz .Lprep_tend
	s_and_b32 s24, s0, 0xffffffc0
	s_mov_b32 s25, s1
	v_add_u32_e32 v31, s24, v25
	v_xor_b32_e32 v31, s0, v31
	v_cmp_gt_u32_e32 vcc, 0x1000, v31
	s_and_b64 exec, exec, vcc
	s_cbranch_execz .Lprep_tend
	global_load_dwordx4 v[32:35], v25, s[24:25]
